# expert counters spread to one 256B line each (router atomics no longer serialise on one line)
# speedup vs baseline: 1.0228x; 1.0228x over previous
; #define LAS __attribute__((address_space(3)))
; __device__ __forceinline__ unsigned xb_add(unsigned* p, unsigned v) { return __hip_atomic_fetch_add(p, v, __ATOMIC_RELAXED, __HIP_MEMORY_SCOPE_AGENT); }
; __device__ __forceinline__ unsigned xb_xcc_id() { return (unsigned)__builtin_amdgcn_s_getreg((3 << 11) | 20) & 0xFu; }
; #define TID() make_tid(wave_s)
; __device__ __forceinline__ XcdBarrier xcd_barrier_post(unsigned* bar, volatile LAS unsigned* st, int tid) {
;     XcdBarrier b; b.bar = bar; b.x = xb_xcc_id(); b.st = st;
;     if (tid == 0) (void)xb_add(&bar[XB_XCNT(b.x)], 1u);
;     return b;
; __global__ void __launch_bounds__(NTHR, 2) fwd_kernel(Args args) {
;     extern __shared__ __attribute__((aligned(16))) unsigned char lds[];
;     LAS unsigned char* ldsl = (LAS unsigned char*)lds;
;     volatile LAS unsigned* MISC = (volatile LAS unsigned*)(ldsl + MISC_OFF);
;     LAS unsigned* TL = (LAS unsigned*)(ldsl + LDSCTL_OFF);
;     const int wave_s = __builtin_amdgcn_readfirstlane(threadIdx.x >> 6);
;     ...
;     { const int t0 = TID(); for (int u = t0; u < (LDS_BYTES - LDSCTL_OFF) / 4; u += NTHR) ((LAS unsigned*)(ldsl + LDSCTL_OFF))[u] = 0u; }
;     __syncthreads();
;     unsigned char* ws = args.ws;
;     unsigned* ctl = (unsigned*)(ws + WS_CTL);
;     XcdBarrier bar; bar.bar = ctl + CW_BAR; bar.x = 0; bar.st = nullptr;
;     const bool one_launch = (args.ph_hi - args.ph_lo) > 1;
;     if (one_launch) bar = xcd_barrier_post(ctl + CW_BAR, MISC + 8, TID());
_Z10fwd_kernel4Args:
	s_load_dwordx16 s[52:67], s[0:1], 0x0
	s_load_dwordx4 s[84:87], s[0:1], 0xe0
	s_mov_b64 s[96:97], s[0:1]
	v_readfirstlane_b32 s0, v0
	v_mbcnt_lo_u32_b32 v0, -1, 0
	v_mbcnt_hi_u32_b32 v0, -1, v0
	s_mov_b32 s83, s2
	v_mov_b32_e32 v1, 0
	v_writelane_b32 v249, s0, 0
	s_and_b32 s0, s0, 0x1c0
	v_writelane_b32 v249, s0, 1
	v_or_b32_e32 v0, s0, v0
	s_mov_b32 s0, 0
	v_writelane_b32 v249, s0, 2
	s_waitcnt lgkmcnt(0)
	s_add_u32 s98, s84, 0x20000
	s_addc_u32 s99, s85, 0
	s_add_u32 s0, s84, 0x4000
	s_addc_u32 s1, s85, 0
	v_writelane_b32 v249, s0, 3
	v_lshl_add_u32 v0, v0, 2, 0
	v_add_u32_e32 v0, 0x23000, v0
	v_writelane_b32 v249, s1, 4
	s_sub_i32 s0, s87, s86
	s_cmp_lt_i32 s0, 2
	s_mov_b32 s0, 0
	ds_write2st64_b32 v0, v1, v1 offset1:8
	s_waitcnt lgkmcnt(0)
	s_barrier
	s_cbranch_scc1 .LBB0_5
	v_mbcnt_lo_u32_b32 v0, -1, 0
	v_mbcnt_hi_u32_b32 v0, -1, v0
	v_readlane_b32 s0, v249, 1
	s_nop 1
	v_or_b32_e32 v0, s0, v0
	s_getreg_b32 s0, hwreg(HW_REG_XCC_ID, 0, 4)
	s_and_b32 s0, s0, 15
	v_cmp_eq_u32_e32 vcc, 0, v0
	v_writelane_b32 v249, s0, 2
	s_and_saveexec_b64 s[4:5], vcc
	s_cbranch_execz .LBB0_4
	s_mov_b64 s[0:1], exec
	v_mbcnt_lo_u32_b32 v0, s0, 0
	v_mbcnt_hi_u32_b32 v0, s1, v0
	v_cmp_eq_u32_e32 vcc, 0, v0
	s_and_b64 s[2:3], exec, vcc
	s_mov_b64 exec, s[2:3]
	s_cbranch_execz .LBB0_4
	v_readlane_b32 s2, v249, 2
	s_bcnt1_i32_b64 s0, s[0:1]
	s_lshl_b32 s2, s2, 8
	v_mov_b32_e32 v1, s0
	v_readlane_b32 s0, v249, 3
	v_mov_b32_e32 v0, s2
	v_readlane_b32 s1, v249, 4
	s_nop 4
	global_atomic_add v0, v1, s[0:1] offset:1024

; #define LDS_WAIT() asm volatile("s_waitcnt lgkmcnt(0)" ::: "memory")
; __device__ __forceinline__ void phase_router(const Args& a, unsigned char* lds_g, int tid, int lane, int wave) {
;     ...
;         __syncthreads();
;         if (wave < 2) { const int slot = wave; const int tok0 = 32 * tp + 16 * slot;
;             const float* sp = SSQP + slot * 128; const float rstd = 1.f / sqrtf((((sp[i] + sp[16 + i]) + (sp[32 + i] + sp[48 + i])) + ((sp[64 + i] + sp[80 + i]) + (sp[96 + i] + sp[112 + i]))) * (1.f / D) + EPS);
;             if (gq == 0) RS[slot * 16 + i] = rstd;
; #pragma unroll
;             for (int cb = 0; cb < 3; ++cb) { const f32x4* pp = PART + (slot * 8 * 3 + cb) * 64 + lane; const f32x4 sum = ((pp[0] + pp[3 * 64]) + (pp[6 * 64] + pp[9 * 64])) + ((pp[12 * 64] + pp[15 * 64]) + (pp[18 * 64] + pp[21 * 64]));
;                 const float rb = RB[b * 48 + 16 * cb + i];
; #pragma unroll
;                 for (int r = 0; r < 4; ++r) LG[(slot * 16 + 4 * gq + r) * 48 + 16 * cb + i] = __shfl(rstd, 4 * gq + r) * sum[r] + rb; }
;             LDS_WAIT(); asm volatile("" ::: "memory");
.LBB0_979:
	s_or_b64 exec, exec, s[4:5]
	s_andn2_b64 vcc, exec, s[26:27]
	s_waitcnt lgkmcnt(0)
	s_barrier
	s_cbranch_vccnz .LBB0_985
	v_add_u32_e32 v4, 0xc000, v178
	ds_read2_b32 v[0:1], v4 offset1:16
	ds_read_b32 v6, v179 offset:49152
	ds_read2_b32 v[2:3], v4 offset0:32 offset1:64
	ds_read2_b32 v[4:5], v4 offset0:80 offset1:96
	ds_read_b32 v7, v180 offset:49152
	s_waitcnt lgkmcnt(4)
	v_add_f32_e32 v0, v0, v1
	s_waitcnt lgkmcnt(2)
	v_add_f32_e32 v1, v2, v6
	v_add_f32_e32 v0, v0, v1
	s_waitcnt lgkmcnt(1)
	v_add_f32_e32 v1, v3, v4
	s_waitcnt lgkmcnt(0)
	v_add_f32_e32 v2, v5, v7
	v_add_f32_e32 v1, v1, v2
	v_add_f32_e32 v0, v0, v1
	v_fmamk_f32 v0, v0, 0x3a000000, v188
	v_mul_f32_e32 v1, 0x4f800000, v0
	v_cmp_gt_f32_e32 vcc, s53, v0
	s_nop 1
	v_cndmask_b32_e32 v0, v0, v1, vcc
	v_sqrt_f32_e32 v1, v0
	s_nop 0
	v_add_u32_e32 v2, -1, v1
	v_fma_f32 v3, -v2, v1, v0
	v_cmp_ge_f32_e64 s[4:5], 0, v3
	v_add_u32_e32 v3, 1, v1
	s_nop 0
	v_cndmask_b32_e64 v2, v1, v2, s[4:5]
	v_fma_f32 v1, -v3, v1, v0
	v_cmp_lt_f32_e64 s[4:5], 0, v1
	s_nop 1
	v_cndmask_b32_e64 v1, v2, v3, s[4:5]
	v_mul_f32_e32 v2, 0x37800000, v1
	v_cndmask_b32_e32 v1, v1, v2, vcc
	v_cmp_class_f32_e32 vcc, v0, v189
	s_nop 1
	v_cndmask_b32_e32 v0, v1, v0, vcc
	v_div_scale_f32 v1, s[4:5], v0, v0, 1.0
	v_rcp_f32_e32 v2, v1
	s_nop 0
	v_fma_f32 v3, -v1, v2, 1.0
	v_fmac_f32_e32 v2, v3, v2
	v_div_scale_f32 v3, vcc, 1.0, v0, 1.0
	v_mul_f32_e32 v4, v3, v2
	v_fma_f32 v5, -v1, v4, v3
	v_fmac_f32_e32 v4, v5, v2
	v_fma_f32 v1, -v1, v4, v3
	v_div_fmas_f32 v1, v1, v2, v4
	v_div_fixup_f32 v0, v1, v0, 1.0
	s_and_saveexec_b64 s[4:5], s[0:1]
	ds_write_b32 v65, v0 offset:50176
	s_or_b64 exec, exec, s[4:5]
	v_lshl_add_u64 v[32:33], v[24:25], 2, s[20:21]
	global_load_dword v34, v[32:33], off
	global_load_dword v40, v[32:33], off offset:64
	v_add_u32_e32 v35, s39, v64
	ds_bpermute_b32 v36, v184, v0
	ds_bpermute_b32 v37, v185, v0
	ds_bpermute_b32 v38, v186, v0
	ds_bpermute_b32 v39, v187, v0
	ds_read_b128 v[0:3], v35
	ds_read_b128 v[4:7], v35 offset:3072
	ds_read_b128 v[8:11], v35 offset:6144
	ds_read_b128 v[12:15], v35 offset:9216
	ds_read_b128 v[16:19], v35 offset:12288
	ds_read_b128 v[20:23], v35 offset:15360
	ds_read_b128 v[24:27], v35 offset:18432
	ds_read_b128 v[28:31], v35 offset:21504
	global_load_dword v32, v[32:33], off offset:128
	s_waitcnt lgkmcnt(6)
	v_add_f32_e32 v0, v0, v4
	s_waitcnt lgkmcnt(4)
	v_add_f32_e32 v4, v8, v12
	s_waitcnt lgkmcnt(2)
	v_add_f32_e32 v8, v16, v20
	s_waitcnt lgkmcnt(0)
	v_add_f32_e32 v12, v24, v28
	v_add_f32_e32 v1, v1, v5
	v_add_f32_e32 v5, v9, v13
	v_add_f32_e32 v9, v17, v21
	v_add_f32_e32 v13, v25, v29
	v_add_f32_e32 v2, v2, v6
	v_add_f32_e32 v6, v10, v14
	v_add_f32_e32 v10, v18, v22
	v_add_f32_e32 v14, v26, v30
	v_add_f32_e32 v3, v3, v7
	v_add_f32_e32 v7, v11, v15
	v_add_f32_e32 v11, v19, v23
	v_add_f32_e32 v15, v27, v31
	v_add_f32_e32 v0, v0, v4
	v_add_f32_e32 v4, v8, v12
	v_add_f32_e32 v1, v1, v5
	v_add_f32_e32 v5, v9, v13
	v_add_f32_e32 v2, v2, v6
	v_add_f32_e32 v6, v10, v14
	v_add_f32_e32 v3, v3, v7
	v_add_f32_e32 v7, v11, v15
	v_add_f32_e32 v0, v0, v4
	v_add_f32_e32 v1, v1, v5
	v_add_f32_e32 v2, v2, v6
	v_add_f32_e32 v3, v3, v7
	s_waitcnt vmcnt(2)
	v_fma_f32 v0, v0, v36, v34
	v_fma_f32 v1, v1, v37, v34
	v_fma_f32 v2, v2, v38, v34
	v_fmac_f32_e32 v34, v3, v39
	ds_write_b32 v190, v0 offset:51200
	ds_write_b32 v190, v1 offset:51392
	ds_write_b32 v190, v2 offset:51584
	ds_write_b32 v190, v34 offset:51776
	ds_read_b128 v[0:3], v35 offset:1024
	ds_read_b128 v[4:7], v35 offset:4096
	ds_read_b128 v[8:11], v35 offset:7168
	ds_read_b128 v[12:15], v35 offset:10240
	ds_read_b128 v[16:19], v35 offset:13312
	ds_read_b128 v[20:23], v35 offset:16384
	ds_read_b128 v[24:27], v35 offset:19456
	ds_read_b128 v[28:31], v35 offset:22528
	s_waitcnt lgkmcnt(6)
	v_add_f32_e32 v0, v0, v4
	s_waitcnt lgkmcnt(4)
	v_add_f32_e32 v4, v8, v12
	s_waitcnt lgkmcnt(2)
	v_add_f32_e32 v8, v16, v20
	v_add_f32_e32 v1, v1, v5
	s_waitcnt lgkmcnt(0)
	v_add_f32_e32 v12, v24, v28
	v_add_f32_e32 v5, v9, v13
	v_add_f32_e32 v9, v17, v21
	v_add_f32_e32 v13, v25, v29
	v_add_f32_e32 v2, v2, v6
	v_add_f32_e32 v6, v10, v14
	v_add_f32_e32 v10, v18, v22
	v_add_f32_e32 v14, v26, v30
	v_add_f32_e32 v0, v0, v4
	v_add_f32_e32 v4, v8, v12
	v_add_f32_e32 v1, v1, v5
	v_add_f32_e32 v5, v9, v13
	v_add_f32_e32 v2, v2, v6
	v_add_f32_e32 v6, v10, v14
	v_add_f32_e32 v0, v0, v4
	v_add_f32_e32 v3, v3, v7
	v_add_f32_e32 v7, v11, v15
	v_add_f32_e32 v11, v19, v23
	v_add_f32_e32 v15, v27, v31
	v_add_f32_e32 v1, v1, v5
	v_add_f32_e32 v2, v2, v6
	s_waitcnt vmcnt(1)
	v_fma_f32 v0, v0, v36, v40
	v_add_f32_e32 v3, v3, v7
	v_fma_f32 v1, v1, v37, v40
	v_fma_f32 v2, v2, v38, v40
	ds_write_b32 v190, v0 offset:51264
	ds_write_b32 v190, v1 offset:51456
	ds_write_b32 v190, v2 offset:51648
	v_add_f32_e32 v0, v11, v15
	v_add_f32_e32 v0, v3, v0
	v_fmac_f32_e32 v40, v0, v39
	ds_write_b32 v190, v40 offset:51840
	ds_read_b128 v[0:3], v35 offset:2048
	ds_read_b128 v[4:7], v35 offset:5120
	ds_read_b128 v[8:11], v35 offset:8192
	ds_read_b128 v[12:15], v35 offset:11264
	ds_read_b128 v[16:19], v35 offset:14336
	ds_read_b128 v[20:23], v35 offset:17408
	ds_read_b128 v[24:27], v35 offset:20480
	ds_read_b128 v[28:31], v35 offset:23552
	s_waitcnt lgkmcnt(6)
	v_add_f32_e32 v0, v0, v4
	s_waitcnt lgkmcnt(4)
	v_add_f32_e32 v4, v8, v12
	v_add_f32_e32 v0, v0, v4
	s_waitcnt lgkmcnt(2)
	v_add_f32_e32 v4, v16, v20
	s_waitcnt lgkmcnt(0)
	v_add_f32_e32 v8, v24, v28
	v_add_f32_e32 v4, v4, v8
	v_add_f32_e32 v0, v0, v4
	s_waitcnt vmcnt(0)
	v_fma_f32 v0, v0, v36, v32
	ds_write_b32 v190, v0 offset:51328
	v_add_f32_e32 v0, v1, v5
	v_add_f32_e32 v1, v9, v13
	v_add_f32_e32 v0, v0, v1
	v_add_f32_e32 v1, v17, v21
	v_add_f32_e32 v4, v25, v29
	v_add_f32_e32 v1, v1, v4
	v_add_f32_e32 v0, v0, v1
	v_fma_f32 v0, v0, v37, v32
	ds_write_b32 v190, v0 offset:51520
	v_add_f32_e32 v0, v2, v6
	v_add_f32_e32 v1, v10, v14
	v_add_f32_e32 v0, v0, v1
	v_add_f32_e32 v1, v18, v22
	v_add_f32_e32 v2, v26, v30
	v_add_f32_e32 v1, v1, v2
	v_add_f32_e32 v0, v0, v1
	v_fma_f32 v0, v0, v38, v32
	ds_write_b32 v190, v0 offset:51712
	v_add_f32_e32 v0, v3, v7
	v_add_f32_e32 v1, v11, v15
	v_add_f32_e32 v0, v0, v1
	v_add_f32_e32 v1, v19, v23
	v_add_f32_e32 v2, v27, v31
	v_add_f32_e32 v1, v1, v2
	v_add_f32_e32 v0, v0, v1
	v_fmac_f32_e32 v32, v0, v39
	ds_write_b32 v190, v32 offset:51904
	s_waitcnt lgkmcnt(0)
	s_and_saveexec_b64 s[28:29], s[0:1]
	s_cbranch_execz .LBB0_984
; __device__ __forceinline__ void phase_router(const Args& a, unsigned char* lds_g, int tid, int lane, int wave) {
;     ...
;             if (lane < 16) {
;                 const float* lg = LG + (slot * 16 + lane) * 48; const int t = tok0 + lane;
;                 int gs = 0; float gm = lg[32];
; #pragma unroll
;                 for (int q = 1; q < 4; ++q) { const float v = lg[32 + q]; if (v > gm) { gm = v; gs = q; } }
;                 float se = 0.f;
; #pragma unroll
;                 for (int q = 0; q < 4; ++q) se += __expf(lg[32 + q] - gm);
;                 const float pg = 1.f / se;
;                 int i0 = 0; float v0 = lg[gs * 8];
; #pragma unroll
;                 for (int q = 1; q < 8; ++q) { const float v = lg[gs * 8 + q]; if (v > v0) { v0 = v; i0 = q; } }
;                 int i1 = -1; float v1 = -3.0e38f;
; #pragma unroll
;                 for (int q = 0; q < 8; ++q) { const float v = lg[gs * 8 + q]; if (q != i0 && v > v1) { v1 = v; i1 = q; } }
;                 const float e1 = __expf(v1 - v0), w0 = pg / (1.f + e1), w1 = pg * e1 / (1.f + e1);
;                 const int ex0 = gs * 8 + i0, ex1 = gs * 8 + i1;
;                 const unsigned p0 = atomicAdd(cnt + ex0, 1u), p1 = atomicAdd(cnt + ex1, 1u);
;                 ASG[2 * t] = make_int4(ex0, (int)p0, __float_as_int(w0), 0); ASG[2 * t + 1] = make_int4(ex1, (int)p1, __float_as_int(w1), 0);
;                 int* LIST = (int*)(a.ws + WS_LIST); LIST[ex0 * 8192 + (int)p0] = t; LIST[ex1 * 8192 + (int)p1] = t;
;             }
	ds_read_b128 v[0:3], v182 offset:51328
	s_waitcnt lgkmcnt(0)
	v_cmp_gt_f32_e32 vcc, v1, v0
	s_nop 1
	v_cndmask_b32_e32 v4, v0, v1, vcc
	v_cmp_gt_f32_e64 s[4:5], v2, v4
	v_cndmask_b32_e64 v5, 0, 8, vcc
	s_nop 0
	v_cndmask_b32_e64 v4, v4, v2, s[4:5]
	v_cmp_gt_f32_e32 vcc, v3, v4
	s_nop 1
	v_cndmask_b32_e32 v12, v4, v3, vcc
	v_cndmask_b32_e64 v4, v5, 16, s[4:5]
	v_cndmask_b32_e64 v13, v4, 24, vcc
	v_lshl_add_u32 v8, v13, 2, v182
	ds_read_b128 v[4:7], v8 offset:51200
	ds_read_b128 v[8:11], v8 offset:51216
	v_sub_f32_e32 v0, v0, v12
	v_mul_f32_e32 v0, 0x3fb8aa3b, v0
	v_sub_f32_e32 v1, v1, v12
	s_waitcnt lgkmcnt(1)
	v_cmp_gt_f32_e32 vcc, v5, v4
	v_cmp_nlt_f32_e64 s[6:7], s54, v4
	v_exp_f32_e32 v0, v0
	v_cndmask_b32_e32 v14, v4, v5, vcc
	v_cndmask_b32_e64 v15, 0, 1, vcc
	v_cmp_gt_f32_e32 vcc, v6, v14
	v_mul_f32_e32 v1, 0x3fb8aa3b, v1
	v_sub_f32_e32 v2, v2, v12
	v_cndmask_b32_e32 v14, v14, v6, vcc
	v_cndmask_b32_e64 v15, v15, 2, vcc
	v_cmp_gt_f32_e32 vcc, v7, v14
	v_exp_f32_e32 v1, v1
	v_mul_f32_e32 v2, 0x3fb8aa3b, v2
	v_cndmask_b32_e32 v14, v14, v7, vcc
	v_cndmask_b32_e64 v15, v15, 3, vcc
	s_waitcnt lgkmcnt(0)
	v_cmp_gt_f32_e32 vcc, v8, v14
	v_sub_f32_e32 v3, v3, v12
	v_exp_f32_e32 v2, v2
	v_cndmask_b32_e32 v14, v14, v8, vcc
	v_cndmask_b32_e64 v15, v15, 4, vcc
	v_cmp_gt_f32_e32 vcc, v9, v14
	v_mul_f32_e32 v3, 0x3fb8aa3b, v3
	v_exp_f32_e32 v3, v3
	v_cndmask_b32_e32 v14, v14, v9, vcc
	v_cndmask_b32_e64 v15, v15, 5, vcc
	v_cmp_gt_f32_e32 vcc, v10, v14
	v_add_f32_e32 v0, 0, v0
	v_add_f32_e32 v0, v1, v0
	v_cndmask_b32_e32 v14, v14, v10, vcc
	v_cndmask_b32_e64 v15, v15, 6, vcc
	v_cmp_ngt_f32_e32 vcc, v11, v14
	v_add_f32_e32 v0, v2, v0
	v_add_f32_e32 v0, v3, v0
	v_cndmask_b32_e32 v15, 7, v15, vcc
	v_cmp_eq_u32_e64 s[4:5], 0, v15
	s_or_b64 s[4:5], s[4:5], s[6:7]
	v_or_b32_e32 v60, v15, v13
	v_cndmask_b32_e64 v4, v4, v192, s[4:5]
	v_cndmask_b32_e64 v16, 0, -1, s[4:5]
	v_cmp_ne_u32_e64 s[4:5], 1, v15
	v_cmp_gt_f32_e64 s[6:7], v5, v4
	s_and_b64 s[4:5], s[4:5], s[6:7]
	v_cndmask_b32_e64 v4, v4, v5, s[4:5]
	v_cndmask_b32_e64 v5, v16, 1, s[4:5]
	v_cmp_ne_u32_e64 s[4:5], 2, v15
	v_cmp_gt_f32_e64 s[6:7], v6, v4
	s_and_b64 s[4:5], s[4:5], s[6:7]
	v_cndmask_b32_e64 v4, v4, v6, s[4:5]
	v_cndmask_b32_e64 v5, v5, 2, s[4:5]
	v_cmp_ne_u32_e64 s[4:5], 3, v15
	v_cmp_gt_f32_e64 s[6:7], v7, v4
	s_and_b64 s[4:5], s[4:5], s[6:7]
	v_cndmask_b32_e64 v4, v4, v7, s[4:5]
	v_cndmask_b32_e64 v5, v5, 3, s[4:5]
	v_cmp_ne_u32_e64 s[4:5], 4, v15
	v_cmp_gt_f32_e64 s[6:7], v8, v4
	s_and_b64 s[4:5], s[4:5], s[6:7]
	v_cndmask_b32_e64 v4, v4, v8, s[4:5]
	v_cndmask_b32_e64 v5, v5, 4, s[4:5]
	v_cmp_ne_u32_e64 s[4:5], 5, v15
	v_cmp_gt_f32_e64 s[6:7], v9, v4
	s_and_b64 s[4:5], s[4:5], s[6:7]
	v_cndmask_b32_e64 v4, v4, v9, s[4:5]
	v_cndmask_b32_e64 v5, v5, 5, s[4:5]
	v_cmp_ne_u32_e64 s[4:5], 6, v15
	v_cmp_gt_f32_e64 s[6:7], v10, v4
	s_and_b64 s[4:5], s[4:5], s[6:7]
	v_cndmask_b32_e64 v4, v4, v10, s[4:5]
	v_cndmask_b32_e64 v5, v5, 6, s[4:5]
	v_cmp_gt_f32_e64 s[4:5], v11, v4
	s_and_b64 s[4:5], vcc, s[4:5]
	v_lshlrev_b32_e32 v6, 8, v60
	v_cndmask_b32_e64 v8, v4, v11, s[4:5]
	v_cndmask_b32_e64 v4, v5, 7, s[4:5]
	v_add_u32_e32 v4, v4, v13
	v_ashrrev_i32_e32 v5, 31, v4
	global_atomic_add v9, v6, v191, s[98:99] sc0
	v_lshlrev_b32_e32 v6, 8, v4
	global_atomic_add v5, v6, v191, s[98:99] sc0
	v_div_scale_f32 v1, s[4:5], v0, v0, 1.0
	v_rcp_f32_e32 v2, v1
	v_cndmask_b32_e32 v3, v11, v14, vcc
	v_sub_f32_e32 v3, v8, v3
	v_mul_f32_e32 v3, 0x3fb8aa3b, v3
	v_fma_f32 v6, -v1, v2, 1.0
	v_fmac_f32_e32 v2, v6, v2
	v_div_scale_f32 v6, vcc, 1.0, v0, 1.0
	v_mul_f32_e32 v7, v6, v2
	v_fma_f32 v10, -v1, v7, v6
	v_exp_f32_e32 v3, v3
	v_fmac_f32_e32 v7, v10, v2
	v_fma_f32 v1, -v1, v7, v6
	v_div_fmas_f32 v1, v1, v2, v7
	v_div_fixup_f32 v0, v1, v0, 1.0
	v_add_f32_e32 v1, 1.0, v3
	v_div_scale_f32 v2, s[4:5], v1, v1, v0
	v_rcp_f32_e32 v6, v2
	v_mul_f32_e32 v3, v0, v3
	v_or_b32_e32 v12, s31, v181
	v_fma_f32 v7, -v2, v6, 1.0
	v_fmac_f32_e32 v6, v7, v6
	v_div_scale_f32 v7, vcc, v0, v1, v0
	v_mul_f32_e32 v8, v7, v6
	v_fma_f32 v10, -v2, v8, v7
	v_fmac_f32_e32 v8, v10, v6
	v_fma_f32 v2, -v2, v8, v7
	v_div_scale_f32 v7, s[4:5], v1, v1, v3
	v_rcp_f32_e32 v11, v7
	v_div_fmas_f32 v2, v2, v6, v8
	v_div_fixup_f32 v10, v2, v1, v0
	v_mov_b32_e32 v8, v60
	v_fma_f32 v0, -v7, v11, 1.0
	v_fmac_f32_e32 v11, v0, v11
	v_div_scale_f32 v0, vcc, v3, v1, v3
	v_mul_f32_e32 v2, v0, v11
	v_fma_f32 v6, -v7, v2, v0
	v_fmac_f32_e32 v2, v6, v11
	v_fma_f32 v0, -v7, v2, v0
	v_div_fmas_f32 v0, v0, v11, v2
	v_div_fixup_f32 v6, v0, v1, v3
	v_lshlrev_b32_e32 v0, 1, v12
	v_ashrrev_i32_e32 v1, 31, v0
	v_lshl_add_u64 v[0:1], v[0:1], 4, s[22:23]
	v_mov_b32_e32 v11, v61
	v_mov_b32_e32 v7, v61
	s_waitcnt vmcnt(1)
	global_store_dwordx4 v[0:1], v[8:11], off
	s_waitcnt vmcnt(1)
	global_store_dwordx4 v[0:1], v[4:7], off offset:16
	v_lshl_add_u32 v0, v60, 13, v9
	v_ashrrev_i32_e32 v1, 31, v0
	v_lshl_add_u64 v[0:1], v[0:1], 2, s[24:25]
	global_store_dword v[0:1], v12, off
	v_lshl_add_u32 v0, v4, 13, v5
	v_ashrrev_i32_e32 v1, 31, v0
	v_lshl_add_u64 v[0:1], v[0:1], 2, s[24:25]
	global_store_dword v[0:1], v12, off

; __device__ __forceinline__ void moe_tables(const Args& a, unsigned char* lds_g, int tid) {
;     int* cum = (int*)(lds_g + MG_CUM); const unsigned* ctl = (const unsigned*)(a.ws + WS_CTL);
;     if (tid < NEXP) cum[128 + tid] = (int)ctl[CW_CNT + tid];
;     if (tid == 0) { int c = 0; for (int e = 0; e < NEXP; ++e) { cum[e] = c; c += (int)((ctl[CW_CNT + e] + 255u) >> 8); } cum[NEXP] = c; }
;     __syncthreads();
; }
.LBB0_1163:
	s_cmp_lt_i32 s86, 8
	s_cselect_b64 s[2:3], -1, 0
	s_and_b64 s[24:25], s[2:3], s[0:1]
	s_andn2_b64 vcc, exec, s[24:25]
	s_cbranch_vccnz .LBB0_1215
	v_mbcnt_lo_u32_b32 v0, -1, 0
	v_mbcnt_hi_u32_b32 v0, -1, v0
	v_readlane_b32 s0, v249, 1
	s_nop 1
	v_or_b32_e32 v0, s0, v0
	v_cmp_gt_u32_e32 vcc, 32, v0
	s_and_saveexec_b64 s[0:1], vcc
	s_cbranch_execz .LBB0_1166
	v_mov_b32_e32 v1, 0
	v_lshlrev_b32_e32 v2, 8, v0
	global_load_dword v1, v2, s[98:99]
	s_add_i32 s2, 0, 0x22800
	v_lshl_add_u32 v2, v0, 2, s2
	s_waitcnt vmcnt(0)
	ds_write_b32 v2, v1 offset:512
.LBB0_1166:
	s_or_b64 exec, exec, s[0:1]
	s_mov_b32 s27, 0
	v_cmp_eq_u32_e32 vcc, 0, v0
	s_and_saveexec_b64 s[0:1], vcc
	s_cbranch_execz .LBB0_1168
	v_mov_b32_e32 v2, 0
	v_mov_b32_e32 v3, 0x1000
	global_load_dword v4, v2, s[98:99]
	global_load_dword v5, v2, s[98:99] offset:256
	global_load_dword v6, v2, s[98:99] offset:512
	global_load_dword v7, v2, s[98:99] offset:768
	global_load_dword v8, v2, s[98:99] offset:1024
	global_load_dword v9, v2, s[98:99] offset:1280
	global_load_dword v10, v2, s[98:99] offset:1536
	global_load_dword v11, v2, s[98:99] offset:1792
	global_load_dword v12, v2, s[98:99] offset:2048
	global_load_dword v13, v2, s[98:99] offset:2304
	global_load_dword v14, v2, s[98:99] offset:2560
	global_load_dword v15, v2, s[98:99] offset:2816
	global_load_dword v16, v2, s[98:99] offset:3072
	global_load_dword v17, v2, s[98:99] offset:3328
	global_load_dword v18, v2, s[98:99] offset:3584
	global_load_dword v19, v2, s[98:99] offset:3840
	global_load_dword v20, v3, s[98:99]
	global_load_dword v21, v3, s[98:99] offset:256
	global_load_dword v22, v3, s[98:99] offset:512
	global_load_dword v23, v3, s[98:99] offset:768
	global_load_dword v24, v3, s[98:99] offset:1024
	global_load_dword v25, v3, s[98:99] offset:1280
	global_load_dword v26, v3, s[98:99] offset:1536
	global_load_dword v27, v3, s[98:99] offset:1792
	global_load_dword v28, v3, s[98:99] offset:2048
	global_load_dword v29, v3, s[98:99] offset:2304
	global_load_dword v30, v3, s[98:99] offset:2560
	global_load_dword v31, v3, s[98:99] offset:2816
	global_load_dword v32, v3, s[98:99] offset:3072
	global_load_dword v33, v3, s[98:99] offset:3328
	global_load_dword v34, v3, s[98:99] offset:3584
	global_load_dword v35, v3, s[98:99] offset:3840
	s_add_i32 s2, 0, 0x22800
	v_mov_b32_e32 v1, s2
	s_add_i32 s3, 0, 0x22810
	v_mov_b32_e32 v36, s3
	s_add_i32 s4, 0, 0x22820
	v_mov_b32_e32 v37, s4
	s_add_i32 s5, 0, 0x22830
	v_mov_b32_e32 v38, s5
	s_add_i32 s6, 0, 0x22840
	v_mov_b32_e32 v39, s6
	s_add_i32 s7, 0, 0x22850
	v_mov_b32_e32 v40, s7
	s_add_i32 s16, 0, 0x22860
	v_mov_b32_e32 v41, s16
	s_add_i32 s2, 0, 0x22870
	s_waitcnt vmcnt(0)
	v_add_u32_e32 v3, 0xff, v4
	v_add_u32_e32 v4, 0xff, v5
	v_add_u32_e32 v5, 0xff, v6
	v_lshrrev_b32_e32 v3, 8, v3
	v_lshrrev_b32_e32 v4, 8, v4
	v_add_u32_e32 v6, 0xff, v7
	v_lshrrev_b32_e32 v5, 8, v5
	v_add_u32_e32 v4, v4, v3
	v_add_u32_e32 v7, 0xff, v8
	v_lshrrev_b32_e32 v6, 8, v6
	v_add_u32_e32 v5, v5, v4
	v_add_u32_e32 v8, 0xff, v9
	v_lshrrev_b32_e32 v7, 8, v7
	ds_write_b128 v1, v[2:5]
	v_add_u32_e32 v2, v6, v5
	v_add_u32_e32 v9, 0xff, v10
	v_lshrrev_b32_e32 v8, 8, v8
	v_add_u32_e32 v3, v7, v2
	v_add_u32_e32 v10, 0xff, v11
	v_lshrrev_b32_e32 v9, 8, v9
	v_add_u32_e32 v4, v8, v3
	v_add_u32_e32 v11, 0xff, v12
	v_lshrrev_b32_e32 v10, 8, v10
	v_add_u32_e32 v5, v9, v4
	v_add_u32_e32 v12, 0xff, v13
	v_lshrrev_b32_e32 v11, 8, v11
	ds_write_b128 v36, v[2:5]
	v_add_u32_e32 v2, v10, v5
	v_add_u32_e32 v13, 0xff, v14
	v_lshrrev_b32_e32 v12, 8, v12
	v_add_u32_e32 v3, v11, v2
	v_add_u32_e32 v14, 0xff, v15
	v_lshrrev_b32_e32 v13, 8, v13
	v_add_u32_e32 v4, v12, v3
	v_add_u32_e32 v15, 0xff, v16
	v_lshrrev_b32_e32 v14, 8, v14
	v_add_u32_e32 v5, v13, v4
	v_add_u32_e32 v16, 0xff, v17
	v_lshrrev_b32_e32 v15, 8, v15
	ds_write_b128 v37, v[2:5]
	v_add_u32_e32 v2, v14, v5
	v_add_u32_e32 v17, 0xff, v18
	v_lshrrev_b32_e32 v16, 8, v16
	v_add_u32_e32 v3, v15, v2
	v_add_u32_e32 v18, 0xff, v19
	v_lshrrev_b32_e32 v17, 8, v17
	v_add_u32_e32 v4, v16, v3
	v_add_u32_e32 v19, 0xff, v20
	v_lshrrev_b32_e32 v18, 8, v18
	v_add_u32_e32 v5, v17, v4
	v_add_u32_e32 v20, 0xff, v21
	v_lshrrev_b32_e32 v19, 8, v19
	ds_write_b128 v38, v[2:5]
	v_add_u32_e32 v2, v18, v5
	v_add_u32_e32 v21, 0xff, v22
	v_lshrrev_b32_e32 v20, 8, v20
	v_add_u32_e32 v3, v19, v2
	v_add_u32_e32 v22, 0xff, v23
	v_lshrrev_b32_e32 v21, 8, v21
	v_add_u32_e32 v4, v20, v3
	v_add_u32_e32 v23, 0xff, v24
	v_lshrrev_b32_e32 v22, 8, v22
	v_add_u32_e32 v5, v21, v4
	v_add_u32_e32 v24, 0xff, v25
	v_lshrrev_b32_e32 v23, 8, v23
	ds_write_b128 v39, v[2:5]
	v_add_u32_e32 v2, v22, v5
	v_add_u32_e32 v25, 0xff, v26
	v_lshrrev_b32_e32 v24, 8, v24
	v_add_u32_e32 v3, v23, v2
	v_add_u32_e32 v26, 0xff, v27
	v_lshrrev_b32_e32 v25, 8, v25
	v_add_u32_e32 v4, v24, v3
	v_add_u32_e32 v27, 0xff, v28
	v_lshrrev_b32_e32 v26, 8, v26
	v_add_u32_e32 v5, v25, v4
	v_add_u32_e32 v28, 0xff, v29
	v_lshrrev_b32_e32 v27, 8, v27
	ds_write_b128 v40, v[2:5]
	v_add_u32_e32 v2, v26, v5
	v_add_u32_e32 v29, 0xff, v30
	v_lshrrev_b32_e32 v28, 8, v28
	v_add_u32_e32 v3, v27, v2
	v_lshrrev_b32_e32 v29, 8, v29
	v_add_u32_e32 v4, v28, v3
	v_add_u32_e32 v1, 0xff, v31
	v_add_u32_e32 v5, v29, v4
	v_lshrrev_b32_e32 v1, 8, v1
	ds_write_b128 v41, v[2:5]
	v_add_u32_e32 v2, v1, v5
	v_add_u32_e32 v1, 0xff, v32
	v_lshrrev_b32_e32 v1, 8, v1
	v_add_u32_e32 v3, v1, v2
	v_add_u32_e32 v1, 0xff, v33
	v_lshrrev_b32_e32 v1, 8, v1
	v_add_u32_e32 v4, v1, v3
	v_add_u32_e32 v1, 0xff, v34
	v_lshrrev_b32_e32 v1, 8, v1
	v_add_u32_e32 v5, v1, v4
	v_mov_b32_e32 v1, s2
	ds_write_b128 v1, v[2:5]
	v_add_u32_e32 v1, 0xff, v35
	v_lshrrev_b32_e32 v1, 8, v1
	s_add_i32 s2, 0, 0x22880
	v_add_u32_e32 v1, v1, v5
	v_mov_b32_e32 v2, s2
	ds_write_b32 v2, v1

; __device__ __forceinline__ void moe_tables(const Args& a, unsigned char* lds_g, int tid) {
;     int* cum = (int*)(lds_g + MG_CUM); const unsigned* ctl = (const unsigned*)(a.ws + WS_CTL);
;     if (tid < NEXP) cum[128 + tid] = (int)ctl[CW_CNT + tid];
;     if (tid == 0) { int c = 0; for (int e = 0; e < NEXP; ++e) { cum[e] = c; c += (int)((ctl[CW_CNT + e] + 255u) >> 8); } cum[NEXP] = c; }
;     __syncthreads();
; }
.LBB0_1265:
	s_cmp_lt_i32 s86, 9
	s_cselect_b64 s[2:3], -1, 0
	s_and_b64 s[4:5], s[2:3], s[0:1]
	s_andn2_b64 vcc, exec, s[4:5]
	s_cbranch_vccnz .LBB0_1281
	v_readlane_b32 s0, v249, 1
	v_mbcnt_lo_u32_b32 v0, -1, 0
	v_mbcnt_hi_u32_b32 v0, -1, v0
	s_nop 1
	v_or_b32_e32 v2, s0, v0
	v_cmp_gt_u32_e32 vcc, 32, v2
	v_readfirstlane_b32 s2, v2
	s_and_saveexec_b64 s[0:1], vcc
	s_cbranch_execz .LBB0_1268
	v_mov_b32_e32 v3, 0
	v_lshlrev_b32_e32 v4, 8, v2
	global_load_dword v1, v4, s[98:99]
	s_add_i32 s3, 0, 0x22800
	v_lshl_add_u32 v3, v2, 2, s3
	s_waitcnt vmcnt(0)
	ds_write_b32 v3, v1 offset:512
.LBB0_1268:
	s_or_b64 exec, exec, s[0:1]
	v_cmp_eq_u32_e32 vcc, 0, v2
	s_and_saveexec_b64 s[0:1], vcc
	s_cbranch_execz .LBB0_1270
	v_mov_b32_e32 v2, 0
	v_mov_b32_e32 v3, 0x1000
	global_load_dword v4, v2, s[98:99]
	global_load_dword v5, v2, s[98:99] offset:256
	global_load_dword v6, v2, s[98:99] offset:512
	global_load_dword v7, v2, s[98:99] offset:768
	global_load_dword v8, v2, s[98:99] offset:1024
	global_load_dword v9, v2, s[98:99] offset:1280
	global_load_dword v10, v2, s[98:99] offset:1536
	global_load_dword v11, v2, s[98:99] offset:1792
	global_load_dword v12, v2, s[98:99] offset:2048
	global_load_dword v13, v2, s[98:99] offset:2304
	global_load_dword v14, v2, s[98:99] offset:2560
	global_load_dword v15, v2, s[98:99] offset:2816
	global_load_dword v16, v2, s[98:99] offset:3072
	global_load_dword v17, v2, s[98:99] offset:3328
	global_load_dword v18, v2, s[98:99] offset:3584
	global_load_dword v19, v2, s[98:99] offset:3840
	global_load_dword v20, v3, s[98:99]
	global_load_dword v21, v3, s[98:99] offset:256
	global_load_dword v22, v3, s[98:99] offset:512
	global_load_dword v23, v3, s[98:99] offset:768
	global_load_dword v24, v3, s[98:99] offset:1024
	global_load_dword v25, v3, s[98:99] offset:1280
	global_load_dword v26, v3, s[98:99] offset:1536
	global_load_dword v27, v3, s[98:99] offset:1792
	global_load_dword v28, v3, s[98:99] offset:2048
	global_load_dword v29, v3, s[98:99] offset:2304
	global_load_dword v30, v3, s[98:99] offset:2560
	global_load_dword v31, v3, s[98:99] offset:2816
	global_load_dword v32, v3, s[98:99] offset:3072
	global_load_dword v33, v3, s[98:99] offset:3328
	global_load_dword v34, v3, s[98:99] offset:3584
	global_load_dword v35, v3, s[98:99] offset:3840
	s_add_i32 s3, 0, 0x22800
	v_mov_b32_e32 v1, s3
	s_add_i32 s6, 0, 0x22810
	v_mov_b32_e32 v36, s6
	s_add_i32 s7, 0, 0x22820
	v_mov_b32_e32 v37, s7
	s_add_i32 s8, 0, 0x22830
	v_mov_b32_e32 v38, s8
	s_add_i32 s9, 0, 0x22840
	v_mov_b32_e32 v39, s9
	s_add_i32 s10, 0, 0x22850
	s_waitcnt vmcnt(0)
	v_mov_b32_e32 v40, s10
	s_add_i32 s11, 0, 0x22860
	v_mov_b32_e32 v41, s11
	s_add_i32 s3, 0, 0x22870
	v_add_u32_e32 v3, 0xff, v4
	v_add_u32_e32 v4, 0xff, v5
	v_add_u32_e32 v5, 0xff, v6
	v_lshrrev_b32_e32 v3, 8, v3
	v_lshrrev_b32_e32 v4, 8, v4
	v_add_u32_e32 v6, 0xff, v7
	v_lshrrev_b32_e32 v5, 8, v5
	v_add_u32_e32 v4, v4, v3
	v_add_u32_e32 v7, 0xff, v8
	v_lshrrev_b32_e32 v6, 8, v6
	v_add_u32_e32 v5, v5, v4
	v_add_u32_e32 v8, 0xff, v9
	v_lshrrev_b32_e32 v7, 8, v7
	ds_write_b128 v1, v[2:5]
	v_add_u32_e32 v2, v6, v5
	v_add_u32_e32 v9, 0xff, v10
	v_lshrrev_b32_e32 v8, 8, v8
	v_add_u32_e32 v3, v7, v2
	v_add_u32_e32 v10, 0xff, v11
	v_lshrrev_b32_e32 v9, 8, v9
	v_add_u32_e32 v4, v8, v3
	v_add_u32_e32 v11, 0xff, v12
	v_lshrrev_b32_e32 v10, 8, v10
	v_add_u32_e32 v5, v9, v4
	v_add_u32_e32 v12, 0xff, v13
	v_lshrrev_b32_e32 v11, 8, v11
	ds_write_b128 v36, v[2:5]
	v_add_u32_e32 v2, v10, v5
	v_add_u32_e32 v13, 0xff, v14
	v_lshrrev_b32_e32 v12, 8, v12
	v_add_u32_e32 v3, v11, v2
	v_add_u32_e32 v14, 0xff, v15
	v_lshrrev_b32_e32 v13, 8, v13
	v_add_u32_e32 v4, v12, v3
	v_add_u32_e32 v15, 0xff, v16
	v_lshrrev_b32_e32 v14, 8, v14
	v_add_u32_e32 v5, v13, v4
	v_add_u32_e32 v16, 0xff, v17
	v_lshrrev_b32_e32 v15, 8, v15
	ds_write_b128 v37, v[2:5]
	v_add_u32_e32 v2, v14, v5
	v_add_u32_e32 v17, 0xff, v18
	v_lshrrev_b32_e32 v16, 8, v16
	v_add_u32_e32 v3, v15, v2
	v_add_u32_e32 v18, 0xff, v19
	v_lshrrev_b32_e32 v17, 8, v17
	v_add_u32_e32 v4, v16, v3
	v_add_u32_e32 v19, 0xff, v20
	v_lshrrev_b32_e32 v18, 8, v18
	v_add_u32_e32 v5, v17, v4
	v_add_u32_e32 v20, 0xff, v21
	v_lshrrev_b32_e32 v19, 8, v19
	ds_write_b128 v38, v[2:5]
	v_add_u32_e32 v2, v18, v5
	v_add_u32_e32 v21, 0xff, v22
	v_lshrrev_b32_e32 v20, 8, v20
	v_add_u32_e32 v3, v19, v2
	v_add_u32_e32 v22, 0xff, v23
	v_lshrrev_b32_e32 v21, 8, v21
	v_add_u32_e32 v4, v20, v3
	v_add_u32_e32 v23, 0xff, v24
	v_lshrrev_b32_e32 v22, 8, v22
	v_add_u32_e32 v5, v21, v4
	v_add_u32_e32 v24, 0xff, v25
	v_lshrrev_b32_e32 v23, 8, v23
	ds_write_b128 v39, v[2:5]
	v_add_u32_e32 v2, v22, v5
	v_add_u32_e32 v25, 0xff, v26
	v_lshrrev_b32_e32 v24, 8, v24
	v_add_u32_e32 v3, v23, v2
	v_add_u32_e32 v26, 0xff, v27
	v_lshrrev_b32_e32 v25, 8, v25
	v_add_u32_e32 v4, v24, v3
	v_add_u32_e32 v27, 0xff, v28
	v_lshrrev_b32_e32 v26, 8, v26
	v_add_u32_e32 v5, v25, v4
	v_add_u32_e32 v28, 0xff, v29
	v_lshrrev_b32_e32 v27, 8, v27
	ds_write_b128 v40, v[2:5]
	v_add_u32_e32 v2, v26, v5
	v_add_u32_e32 v29, 0xff, v30
	v_lshrrev_b32_e32 v28, 8, v28
	v_add_u32_e32 v3, v27, v2
	v_lshrrev_b32_e32 v29, 8, v29
	v_add_u32_e32 v4, v28, v3
	v_add_u32_e32 v1, 0xff, v31
	v_add_u32_e32 v5, v29, v4
	v_lshrrev_b32_e32 v1, 8, v1
	ds_write_b128 v41, v[2:5]
	v_add_u32_e32 v2, v1, v5
	v_add_u32_e32 v1, 0xff, v32
	v_lshrrev_b32_e32 v1, 8, v1
	v_add_u32_e32 v3, v1, v2
	v_add_u32_e32 v1, 0xff, v33
	v_lshrrev_b32_e32 v1, 8, v1
	v_add_u32_e32 v4, v1, v3
	v_add_u32_e32 v1, 0xff, v34
	v_lshrrev_b32_e32 v1, 8, v1
	v_add_u32_e32 v5, v1, v4
	v_mov_b32_e32 v1, s3
	ds_write_b128 v1, v[2:5]
	v_add_u32_e32 v1, 0xff, v35
	v_lshrrev_b32_e32 v1, 8, v1
	s_add_i32 s3, 0, 0x22880
	v_add_u32_e32 v1, v1, v5
	v_mov_b32_e32 v2, s3
	ds_write_b32 v2, v1

; __global__ void __launch_bounds__(NTHR, 2) fwd_kernel(Args args) {
;     extern __shared__ __attribute__((aligned(16))) unsigned char lds[];
	.amdhsa_kernel _Z10fwd_kernel4Args
		.amdhsa_group_segment_fixed_size 0
		.amdhsa_private_segment_fixed_size 0
		.amdhsa_kernarg_size 496
		.amdhsa_user_sgpr_count 2
		.amdhsa_user_sgpr_dispatch_ptr 0
		.amdhsa_user_sgpr_queue_ptr 0
		.amdhsa_user_sgpr_kernarg_segment_ptr 1
		.amdhsa_user_sgpr_dispatch_id 0
		.amdhsa_user_sgpr_kernarg_preload_length 0
		.amdhsa_user_sgpr_kernarg_preload_offset 0
		.amdhsa_user_sgpr_private_segment_size 0
		.amdhsa_uses_dynamic_stack 0
		.amdhsa_enable_private_segment 0
		.amdhsa_system_sgpr_workgroup_id_x 1
		.amdhsa_system_sgpr_workgroup_id_y 0
		.amdhsa_system_sgpr_workgroup_id_z 0
		.amdhsa_system_sgpr_workgroup_info 0
		.amdhsa_system_vgpr_workitem_id 0
		.amdhsa_next_free_vgpr 250
		.amdhsa_next_free_sgpr 102
		.amdhsa_accum_offset 252
		.amdhsa_reserve_vcc 1
		.amdhsa_float_round_mode_32 0
		.amdhsa_float_round_mode_16_64 0
		.amdhsa_float_denorm_mode_32 3
		.amdhsa_float_denorm_mode_16_64 3
		.amdhsa_dx10_clamp 1
		.amdhsa_ieee_mode 1
		.amdhsa_fp16_overflow 0
		.amdhsa_tg_split 0
		.amdhsa_exception_fp_ieee_invalid_op 0
		.amdhsa_exception_fp_denorm_src 0
		.amdhsa_exception_fp_ieee_div_zero 0
		.amdhsa_exception_fp_ieee_overflow 0
		.amdhsa_exception_fp_ieee_underflow 0
		.amdhsa_exception_fp_ieee_inexact 0
		.amdhsa_exception_int_div_zero 0
	.end_amdhsa_kernel

; __global__ void __launch_bounds__(NTHR, 2) fwd_kernel(Args args) {
;     extern __shared__ __attribute__((aligned(16))) unsigned char lds[];
amdhsa.kernels:
  - .agpr_count:     0
    .args:
      - .offset:         0
        .size:           240
        .value_kind:     by_value
      - .offset:         240
        .size:           4
        .value_kind:     hidden_block_count_x
      - .offset:         244
        .size:           4
        .value_kind:     hidden_block_count_y
      - .offset:         248
        .size:           4
        .value_kind:     hidden_block_count_z
      - .offset:         252
        .size:           2
        .value_kind:     hidden_group_size_x
      - .offset:         254
        .size:           2
        .value_kind:     hidden_group_size_y
      - .offset:         256
        .size:           2
        .value_kind:     hidden_group_size_z
      - .offset:         258
        .size:           2
        .value_kind:     hidden_remainder_x
      - .offset:         260
        .size:           2
        .value_kind:     hidden_remainder_y
      - .offset:         262
        .size:           2
        .value_kind:     hidden_remainder_z
      - .offset:         280
        .size:           8
        .value_kind:     hidden_global_offset_x
      - .offset:         288
        .size:           8
        .value_kind:     hidden_global_offset_y
      - .offset:         296
        .size:           8
        .value_kind:     hidden_global_offset_z
      - .offset:         304
        .size:           2
        .value_kind:     hidden_grid_dims
      - .offset:         360
        .size:           4
        .value_kind:     hidden_dynamic_lds_size
    .group_segment_fixed_size: 0
    .kernarg_segment_align: 8
    .kernarg_segment_size: 496
    .language:       OpenCL C
    .language_version:
      - 2
      - 0
    .max_flat_workgroup_size: 512
    .name:           _Z10fwd_kernel4Args
    .private_segment_fixed_size: 0
    .sgpr_count:     108
    .sgpr_spill_count: 42
    .symbol:         _Z10fwd_kernel4Args.kd
    .uniform_work_group_size: 1
    .uses_dynamic_stack: false
    .vgpr_count:     250
    .vgpr_spill_count: 0
    .wavefront_size: 64
